# v43 + write-through (nt sc1) stores for the GEMM2 Y output
# baseline (speedup 1.0000x reference)
; #define LAS __attribute__((address_space(3)))
;     __device__ __forceinline__ void operator()(const f32x4 (&acc)[2][2][4][2], const Unit& u, int wr, int wc, int fr, int fq) const {
;         const int lane = fq * 16 + fr, wv = wr * 4 + wc;
;         constexpr int B0 = 3 * pg8::HTB, B1 = UT_TOK;
;         const int wofs = (32 * wr + fr) * 256 + (((4 * wc + fq) ^ fr) << 4);
;         const int rr0 = 8 * wv + (lane >> 4);
;         const int rofs = rr0 * 256 + (((lane & 15) ^ (rr0 & 15)) << 4), rofs4 = (rr0 + 4) * 256 + (((lane & 15) ^ ((rr0 + 4) & 15)) << 4);
;         const int t0 = 64 * (rr0 >> 5) + 16 * ((rr0 >> 4) & 1) + (rr0 & 15);
;         unsigned char* yp = Y + (size_t)u.row0 * D + u.nt * 256 + 16 * (lane & 15);
;         { const u32x4 wa = pack(acc, 0, 0), wb = pack(acc, 0, 1); *(LAS u32x4*)(lds + B0 + wofs) = wa; *(LAS u32x4*)(lds + B0 + wofs + 16 * 256) = wb; }
; #pragma unroll
;         for (int sl = 0; sl < 4; ++sl) { const int ai = sl >> 1, mh = sl & 1;
;             asm volatile("s_waitcnt lgkmcnt(0)" ::: "memory"); __builtin_amdgcn_s_barrier();
;             const int rb = (sl & 1) ? B1 : B0, wb_ = (sl & 1) ? B0 : B1;
;             const u32x4 v0 = *(const LAS u32x4*)(lds + rb + rofs), v1 = *(const LAS u32x4*)(lds + rb + rofs4);
;             if (sl < 3) { const int a2 = (sl + 1) >> 1, m2 = ((sl + 1) & 1) * 2;
;                 const u32x4 wa = pack(acc, a2, m2), wb = pack(acc, a2, m2 + 1); *(LAS u32x4*)(lds + wb_ + wofs) = wa; *(LAS u32x4*)(lds + wb_ + wofs + 16 * 256) = wb; }
;             const int rl = ai * 128 + mh * 32 + t0;
;             if (!nost) { if (rl < u.nv) __builtin_nontemporal_store(v0, (u32x4*)(yp + (size_t)rl * D)); if (rl + 4 < u.nv) __builtin_nontemporal_store(v1, (u32x4*)(yp + (size_t)(rl + 4) * D)); } }
.LBB0_845:
	s_nop 15
	s_nop 15
	ds_write_b128 v207, v[172:175] offset:49152
	ds_write_b128 v207, v[168:171] offset:53248
	v_mov_b32_e32 v14, 0
	v_mov_b32_e32 v16, 0
	s_ashr_i32 s89, s88, 31
	s_lshl_b64 s[4:5], s[88:89], 10
	s_add_u32 s4, s18, s4
	s_addc_u32 s5, s19, s5
	s_lshl_b32 s34, s34, 8
	s_waitcnt lgkmcnt(0)
	s_barrier
	ds_read_b128 v[6:9], v231 offset:49152
	ds_read_b128 v[2:5], v235 offset:49152
	s_ashr_i32 s35, s34, 31
	s_add_u32 s4, s4, s34
	s_addc_u32 s5, s5, s35
	v_lshl_add_u64 v[10:11], s[4:5], 0, v[204:205]
	v_add_u32_e32 v12, 0x20410, v207
	v_cmp_gt_i32_e32 vcc, s7, v206
	ds_write_b128 v12, v[144:147]
	ds_write_b128 v211, v[116:119]
	s_and_saveexec_b64 s[4:5], vcc
	s_cbranch_execz .LBB0_847
	v_lshl_add_u64 v[14:15], v[10:11], 0, v[208:209]
	s_waitcnt lgkmcnt(0)
	global_store_dwordx4 v[14:15], v[6:9], off nt sc1
.LBB0_847:
	s_or_b64 exec, exec, s[4:5]
	v_cmp_gt_i32_e32 vcc, s7, v210
	s_and_saveexec_b64 s[4:5], vcc
	s_cbranch_execz .LBB0_849
	s_waitcnt lgkmcnt(0)
	v_lshl_add_u64 v[6:7], v[10:11], 0, v[212:213]
	global_store_dwordx4 v[6:7], v[2:5], off nt sc1
.LBB0_849:
	s_or_b64 exec, exec, s[4:5]
	s_waitcnt lgkmcnt(0)
	s_nop 0
	v_med3_f32 v3, v124, s29, v227
	v_med3_f32 v5, v125, s29, v227
	v_cvt_pk_fp8_f32 v15, v3, v5
	v_med3_f32 v2, v128, s29, v227
	v_med3_f32 v4, v129, s29, v227
	v_mov_b32_e32 v14, 0
	v_cvt_pk_fp8_f32 v14, v2, v4
	v_med3_f32 v7, v126, s29, v227
	v_med3_f32 v2, v127, s29, v227
	v_med3_f32 v3, v156, s29, v227
	v_med3_f32 v5, v157, s29, v227
	v_cvt_pk_fp8_f32 v15, v7, v2 op_sel:[0,0,1]
	v_cvt_pk_fp8_f32 v17, v3, v5
	v_med3_f32 v2, v160, s29, v227
	v_med3_f32 v4, v161, s29, v227
	v_mov_b32_e32 v16, 0
	v_cvt_pk_fp8_f32 v16, v2, v4
	v_med3_f32 v7, v158, s29, v227
	v_med3_f32 v2, v159, s29, v227
	v_med3_f32 v3, v104, s29, v227
	v_med3_f32 v5, v105, s29, v227
	v_cvt_pk_fp8_f32 v17, v7, v2 op_sel:[0,0,1]
	v_cvt_pk_fp8_f32 v19, v3, v5
	v_med3_f32 v2, v108, s29, v227
	v_med3_f32 v4, v109, s29, v227
	v_cvt_pk_fp8_f32 v18, v2, v4
	v_med3_f32 v6, v130, s29, v227
	v_med3_f32 v8, v131, s29, v227
	v_med3_f32 v7, v106, s29, v227
	v_med3_f32 v2, v107, s29, v227
	v_cvt_pk_fp8_f32 v14, v6, v8 op_sel:[0,0,1]
	v_cvt_pk_fp8_f32 v19, v7, v2 op_sel:[0,0,1]
	v_med3_f32 v6, v162, s29, v227
	v_med3_f32 v8, v163, s29, v227
	v_med3_f32 v2, v140, s29, v227
	v_med3_f32 v3, v132, s29, v227
	v_med3_f32 v4, v141, s29, v227
	v_med3_f32 v5, v133, s29, v227
	v_cvt_pk_fp8_f32 v16, v6, v8 op_sel:[0,0,1]
	v_cvt_pk_fp8_f32 v20, v2, v4
	v_cvt_pk_fp8_f32 v21, v3, v5
	v_med3_f32 v6, v110, s29, v227
	v_med3_f32 v8, v111, s29, v227
	v_cvt_pk_fp8_f32 v18, v6, v8 op_sel:[0,0,1]
	v_med3_f32 v6, v142, s29, v227
	v_med3_f32 v7, v134, s29, v227
	v_med3_f32 v8, v143, s29, v227
	v_med3_f32 v2, v135, s29, v227
	s_waitcnt lgkmcnt(0)
	s_barrier
	v_cvt_pk_fp8_f32 v20, v6, v8 op_sel:[0,0,1]
	v_cvt_pk_fp8_f32 v21, v7, v2 op_sel:[0,0,1]
	ds_read_b128 v[6:9], v248
	ds_read_b128 v[2:5], v249
	v_cmp_gt_i32_e32 vcc, s7, v214
	ds_write_b128 v207, v[14:17] offset:49152
	ds_write_b128 v207, v[18:21] offset:53248
	s_and_saveexec_b64 s[4:5], vcc
	s_cbranch_execz .LBB0_851
	v_lshl_add_u64 v[14:15], v[10:11], 0, v[216:217]
	s_waitcnt lgkmcnt(0)
	global_store_dwordx4 v[14:15], v[6:9], off nt sc1
.LBB0_851:
	s_or_b64 exec, exec, s[4:5]
	v_cmp_gt_i32_e32 vcc, s7, v218
	s_and_saveexec_b64 s[4:5], vcc
	s_cbranch_execz .LBB0_853
	s_waitcnt lgkmcnt(0)
	v_lshl_add_u64 v[6:7], v[10:11], 0, v[220:221]
	global_store_dwordx4 v[6:7], v[2:5], off nt sc1
.LBB0_853:
	s_or_b64 exec, exec, s[4:5]
	s_waitcnt lgkmcnt(0)
	s_nop 0
	v_med3_f32 v3, v84, s29, v227
	v_med3_f32 v5, v85, s29, v227
	v_cvt_pk_fp8_f32 v15, v3, v5
	v_med3_f32 v2, v92, s29, v227
	v_med3_f32 v4, v93, s29, v227
	v_mov_b32_e32 v14, 0
	v_cvt_pk_fp8_f32 v14, v2, v4
	v_med3_f32 v7, v86, s29, v227
	v_med3_f32 v2, v87, s29, v227
	v_med3_f32 v3, v96, s29, v227
	v_med3_f32 v5, v97, s29, v227
	v_cvt_pk_fp8_f32 v15, v7, v2 op_sel:[0,0,1]
	v_cvt_pk_fp8_f32 v17, v3, v5
	v_med3_f32 v2, v100, s29, v227
	v_med3_f32 v4, v101, s29, v227
	v_mov_b32_e32 v16, 0
	v_cvt_pk_fp8_f32 v16, v2, v4
	v_med3_f32 v7, v98, s29, v227
	v_med3_f32 v2, v99, s29, v227
	v_med3_f32 v3, v72, s29, v227
	v_med3_f32 v5, v73, s29, v227
	v_cvt_pk_fp8_f32 v17, v7, v2 op_sel:[0,0,1]
	v_cvt_pk_fp8_f32 v19, v3, v5
	v_med3_f32 v2, v76, s29, v227
	v_med3_f32 v4, v77, s29, v227
	v_cvt_pk_fp8_f32 v18, v2, v4
	v_med3_f32 v6, v94, s29, v227
	v_med3_f32 v8, v95, s29, v227
	v_med3_f32 v7, v74, s29, v227
	v_med3_f32 v2, v75, s29, v227
	v_cvt_pk_fp8_f32 v14, v6, v8 op_sel:[0,0,1]
	v_cvt_pk_fp8_f32 v19, v7, v2 op_sel:[0,0,1]
	v_med3_f32 v6, v102, s29, v227
	v_med3_f32 v8, v103, s29, v227
	v_med3_f32 v2, v88, s29, v227
	v_med3_f32 v3, v68, s29, v227
	v_med3_f32 v4, v89, s29, v227
	v_med3_f32 v5, v69, s29, v227
	v_cvt_pk_fp8_f32 v16, v6, v8 op_sel:[0,0,1]
	v_cvt_pk_fp8_f32 v20, v2, v4
	v_cvt_pk_fp8_f32 v21, v3, v5
	v_med3_f32 v6, v78, s29, v227
	v_med3_f32 v8, v79, s29, v227
	v_cvt_pk_fp8_f32 v18, v6, v8 op_sel:[0,0,1]
	v_med3_f32 v6, v90, s29, v227
	v_med3_f32 v7, v70, s29, v227
	v_med3_f32 v8, v91, s29, v227
	v_med3_f32 v2, v71, s29, v227
	s_waitcnt lgkmcnt(0)
	s_barrier
	v_cvt_pk_fp8_f32 v20, v6, v8 op_sel:[0,0,1]
	v_cvt_pk_fp8_f32 v21, v7, v2 op_sel:[0,0,1]
	ds_read_b128 v[6:9], v231 offset:49152
	ds_read_b128 v[2:5], v235 offset:49152
	v_cmp_gt_i32_e32 vcc, s7, v222
	ds_write_b128 v12, v[14:17]
	ds_write_b128 v211, v[18:21]
	s_and_saveexec_b64 s[4:5], vcc
	s_cbranch_execz .LBB0_855
	v_lshl_add_u64 v[12:13], v[10:11], 0, v[224:225]
	s_waitcnt lgkmcnt(0)
	global_store_dwordx4 v[12:13], v[6:9], off nt sc1
.LBB0_855:
	s_or_b64 exec, exec, s[4:5]
	v_cmp_gt_i32_e32 vcc, s7, v226
	s_and_saveexec_b64 s[4:5], vcc
	s_cbranch_execz .LBB0_857
	s_waitcnt lgkmcnt(0)
	v_lshl_add_u64 v[6:7], v[10:11], 0, v[228:229]
	global_store_dwordx4 v[6:7], v[2:5], off nt sc1

;     __device__ __forceinline__ void operator()(const f32x4 (&acc)[2][2][4][2], const Unit& u, int wr, int wc, int fr, int fq) const {
;     ...
;             const int rl = ai * 128 + mh * 32 + t0;
;             if (!nost) { if (rl < u.nv) __builtin_nontemporal_store(v0, (u32x4*)(yp + (size_t)rl * D)); if (rl + 4 < u.nv) __builtin_nontemporal_store(v1, (u32x4*)(yp + (size_t)(rl + 4) * D)); } }
.LBB0_860:
	ds_read_b128 v[6:9], v248
	v_lshl_add_u64 v[12:13], v[10:11], 0, v[232:233]
	s_waitcnt lgkmcnt(0)
	global_store_dwordx4 v[12:13], v[6:9], off nt sc1
	s_or_b64 exec, exec, s[4:5]
	v_cmp_gt_i32_e32 vcc, s7, v234
	s_and_saveexec_b64 s[4:5], vcc
	s_cbranch_execz .LBB0_859
.LBB0_861:
	v_lshl_add_u64 v[6:7], v[10:11], 0, v[236:237]
	s_waitcnt lgkmcnt(0)
	global_store_dwordx4 v[6:7], v[2:5], off nt sc1
	s_or_b64 exec, exec, s[4:5]
	s_cmp_eq_u32 s6, s17
	s_mov_b64 s[4:5], -1
	s_cbranch_scc1 .LBB0_835

; #define LAS __attribute__((address_space(3)))
;     __device__ __forceinline__ void operator()(const f32x4 (&acc)[2][2][4][2], const Unit& u, int wr, int wc, int fr, int fq) const {
;         const int lane = fq * 16 + fr, wv = wr * 4 + wc;
;         constexpr int B0 = 3 * pg8::HTB, B1 = UT_TOK;
;         const int wofs = (32 * wr + fr) * 256 + (((4 * wc + fq) ^ fr) << 4);
;         const int rr0 = 8 * wv + (lane >> 4);
;         const int rofs = rr0 * 256 + (((lane & 15) ^ (rr0 & 15)) << 4), rofs4 = (rr0 + 4) * 256 + (((lane & 15) ^ ((rr0 + 4) & 15)) << 4);
;         const int t0 = 64 * (rr0 >> 5) + 16 * ((rr0 >> 4) & 1) + (rr0 & 15);
;         unsigned char* yp = Y + (size_t)u.row0 * D + u.nt * 256 + 16 * (lane & 15);
;         { const u32x4 wa = pack(acc, 0, 0), wb = pack(acc, 0, 1); *(LAS u32x4*)(lds + B0 + wofs) = wa; *(LAS u32x4*)(lds + B0 + wofs + 16 * 256) = wb; }
; #pragma unroll
;         for (int sl = 0; sl < 4; ++sl) { const int ai = sl >> 1, mh = sl & 1;
;             asm volatile("s_waitcnt lgkmcnt(0)" ::: "memory"); __builtin_amdgcn_s_barrier();
;             const int rb = (sl & 1) ? B1 : B0, wb_ = (sl & 1) ? B0 : B1;
;             const u32x4 v0 = *(const LAS u32x4*)(lds + rb + rofs), v1 = *(const LAS u32x4*)(lds + rb + rofs4);
;             if (sl < 3) { const int a2 = (sl + 1) >> 1, m2 = ((sl + 1) & 1) * 2;
;                 const u32x4 wa = pack(acc, a2, m2), wb = pack(acc, a2, m2 + 1); *(LAS u32x4*)(lds + wb_ + wofs) = wa; *(LAS u32x4*)(lds + wb_ + wofs + 16 * 256) = wb; }
;             const int rl = ai * 128 + mh * 32 + t0;
;             if (!nost) { if (rl < u.nv) __builtin_nontemporal_store(v0, (u32x4*)(yp + (size_t)rl * D)); if (rl + 4 < u.nv) __builtin_nontemporal_store(v1, (u32x4*)(yp + (size_t)(rl + 4) * D)); } }
.LBB0_1072:
	s_nop 15
	s_nop 15
	ds_write_b128 v207, v[172:175] offset:49152
	ds_write_b128 v207, v[168:171] offset:53248
	v_mov_b32_e32 v14, 0
	v_mov_b32_e32 v16, 0
	s_ashr_i32 s87, s86, 31
	s_lshl_b64 s[4:5], s[86:87], 10
	s_add_u32 s4, s17, s4
	s_addc_u32 s5, s20, s5
	s_lshl_b32 s18, s34, 8
	s_waitcnt lgkmcnt(0)
	s_barrier
	ds_read_b128 v[6:9], v231 offset:49152
	ds_read_b128 v[2:5], v235 offset:49152
	s_ashr_i32 s19, s18, 31
	s_add_u32 s4, s4, s18
	s_addc_u32 s5, s5, s19
	v_lshl_add_u64 v[10:11], s[4:5], 0, v[204:205]
	v_add_u32_e32 v12, 0x20410, v207
	v_cmp_gt_i32_e32 vcc, s6, v206
	ds_write_b128 v12, v[144:147]
	ds_write_b128 v211, v[116:119]
	s_and_saveexec_b64 s[4:5], vcc
	s_cbranch_execz .LBB0_1074
	v_lshl_add_u64 v[14:15], v[10:11], 0, v[208:209]
	s_waitcnt lgkmcnt(0)
	global_store_dwordx4 v[14:15], v[6:9], off nt sc1
.LBB0_1074:
	s_or_b64 exec, exec, s[4:5]
	v_cmp_gt_i32_e32 vcc, s6, v210
	s_and_saveexec_b64 s[4:5], vcc
	s_cbranch_execz .LBB0_1076
	s_waitcnt lgkmcnt(0)
	v_lshl_add_u64 v[6:7], v[10:11], 0, v[212:213]
	global_store_dwordx4 v[6:7], v[2:5], off nt sc1
.LBB0_1076:
	s_or_b64 exec, exec, s[4:5]
	s_waitcnt lgkmcnt(0)
	s_nop 0
	v_med3_f32 v3, v124, s30, v227
	v_med3_f32 v5, v125, s30, v227
	v_cvt_pk_fp8_f32 v15, v3, v5
	v_med3_f32 v2, v128, s30, v227
	v_med3_f32 v4, v129, s30, v227
	v_mov_b32_e32 v14, 0
	v_cvt_pk_fp8_f32 v14, v2, v4
	v_med3_f32 v7, v126, s30, v227
	v_med3_f32 v2, v127, s30, v227
	v_med3_f32 v3, v156, s30, v227
	v_med3_f32 v5, v157, s30, v227
	v_cvt_pk_fp8_f32 v15, v7, v2 op_sel:[0,0,1]
	v_cvt_pk_fp8_f32 v17, v3, v5
	v_med3_f32 v2, v160, s30, v227
	v_med3_f32 v4, v161, s30, v227
	v_mov_b32_e32 v16, 0
	v_cvt_pk_fp8_f32 v16, v2, v4
	v_med3_f32 v7, v158, s30, v227
	v_med3_f32 v2, v159, s30, v227
	v_med3_f32 v3, v104, s30, v227
	v_med3_f32 v5, v105, s30, v227
	v_cvt_pk_fp8_f32 v17, v7, v2 op_sel:[0,0,1]
	v_cvt_pk_fp8_f32 v19, v3, v5
	v_med3_f32 v2, v108, s30, v227
	v_med3_f32 v4, v109, s30, v227
	v_cvt_pk_fp8_f32 v18, v2, v4
	v_med3_f32 v6, v130, s30, v227
	v_med3_f32 v8, v131, s30, v227
	v_med3_f32 v7, v106, s30, v227
	v_med3_f32 v2, v107, s30, v227
	v_cvt_pk_fp8_f32 v14, v6, v8 op_sel:[0,0,1]
	v_cvt_pk_fp8_f32 v19, v7, v2 op_sel:[0,0,1]
	v_med3_f32 v6, v162, s30, v227
	v_med3_f32 v8, v163, s30, v227
	v_med3_f32 v2, v140, s30, v227
	v_med3_f32 v3, v132, s30, v227
	v_med3_f32 v4, v141, s30, v227
	v_med3_f32 v5, v133, s30, v227
	v_cvt_pk_fp8_f32 v16, v6, v8 op_sel:[0,0,1]
	v_cvt_pk_fp8_f32 v20, v2, v4
	v_cvt_pk_fp8_f32 v21, v3, v5
	v_med3_f32 v6, v110, s30, v227
	v_med3_f32 v8, v111, s30, v227
	v_cvt_pk_fp8_f32 v18, v6, v8 op_sel:[0,0,1]
	v_med3_f32 v6, v142, s30, v227
	v_med3_f32 v7, v134, s30, v227
	v_med3_f32 v8, v143, s30, v227
	v_med3_f32 v2, v135, s30, v227
	s_waitcnt lgkmcnt(0)
	s_barrier
	v_cvt_pk_fp8_f32 v20, v6, v8 op_sel:[0,0,1]
	v_cvt_pk_fp8_f32 v21, v7, v2 op_sel:[0,0,1]
	ds_read_b128 v[6:9], v248
	ds_read_b128 v[2:5], v249
	v_cmp_gt_i32_e32 vcc, s6, v214
	ds_write_b128 v207, v[14:17] offset:49152
	ds_write_b128 v207, v[18:21] offset:53248
	s_and_saveexec_b64 s[4:5], vcc
	s_cbranch_execz .LBB0_1078
	v_lshl_add_u64 v[14:15], v[10:11], 0, v[216:217]
	s_waitcnt lgkmcnt(0)
	global_store_dwordx4 v[14:15], v[6:9], off nt sc1
.LBB0_1078:
	s_or_b64 exec, exec, s[4:5]
	v_cmp_gt_i32_e32 vcc, s6, v218
	s_and_saveexec_b64 s[4:5], vcc
	s_cbranch_execz .LBB0_1080
	s_waitcnt lgkmcnt(0)
	v_lshl_add_u64 v[6:7], v[10:11], 0, v[220:221]
	global_store_dwordx4 v[6:7], v[2:5], off nt sc1
.LBB0_1080:
	s_or_b64 exec, exec, s[4:5]
	s_waitcnt lgkmcnt(0)
	s_nop 0
	v_med3_f32 v3, v84, s30, v227
	v_med3_f32 v5, v85, s30, v227
	v_cvt_pk_fp8_f32 v15, v3, v5
	v_med3_f32 v2, v92, s30, v227
	v_med3_f32 v4, v93, s30, v227
	v_mov_b32_e32 v14, 0
	v_cvt_pk_fp8_f32 v14, v2, v4
	v_med3_f32 v7, v86, s30, v227
	v_med3_f32 v2, v87, s30, v227
	v_med3_f32 v3, v96, s30, v227
	v_med3_f32 v5, v97, s30, v227
	v_cvt_pk_fp8_f32 v15, v7, v2 op_sel:[0,0,1]
	v_cvt_pk_fp8_f32 v17, v3, v5
	v_med3_f32 v2, v100, s30, v227
	v_med3_f32 v4, v101, s30, v227
	v_mov_b32_e32 v16, 0
	v_cvt_pk_fp8_f32 v16, v2, v4
	v_med3_f32 v7, v98, s30, v227
	v_med3_f32 v2, v99, s30, v227
	v_med3_f32 v3, v72, s30, v227
	v_med3_f32 v5, v73, s30, v227
	v_cvt_pk_fp8_f32 v17, v7, v2 op_sel:[0,0,1]
	v_cvt_pk_fp8_f32 v19, v3, v5
	v_med3_f32 v2, v76, s30, v227
	v_med3_f32 v4, v77, s30, v227
	v_cvt_pk_fp8_f32 v18, v2, v4
	v_med3_f32 v6, v94, s30, v227
	v_med3_f32 v8, v95, s30, v227
	v_med3_f32 v7, v74, s30, v227
	v_med3_f32 v2, v75, s30, v227
	v_cvt_pk_fp8_f32 v14, v6, v8 op_sel:[0,0,1]
	v_cvt_pk_fp8_f32 v19, v7, v2 op_sel:[0,0,1]
	v_med3_f32 v6, v102, s30, v227
	v_med3_f32 v8, v103, s30, v227
	v_med3_f32 v2, v88, s30, v227
	v_med3_f32 v3, v68, s30, v227
	v_med3_f32 v4, v89, s30, v227
	v_med3_f32 v5, v69, s30, v227
	v_cvt_pk_fp8_f32 v16, v6, v8 op_sel:[0,0,1]
	v_cvt_pk_fp8_f32 v20, v2, v4
	v_cvt_pk_fp8_f32 v21, v3, v5
	v_med3_f32 v6, v78, s30, v227
	v_med3_f32 v8, v79, s30, v227
	v_cvt_pk_fp8_f32 v18, v6, v8 op_sel:[0,0,1]
	v_med3_f32 v6, v90, s30, v227
	v_med3_f32 v7, v70, s30, v227
	v_med3_f32 v8, v91, s30, v227
	v_med3_f32 v2, v71, s30, v227
	s_waitcnt lgkmcnt(0)
	s_barrier
	v_cvt_pk_fp8_f32 v20, v6, v8 op_sel:[0,0,1]
	v_cvt_pk_fp8_f32 v21, v7, v2 op_sel:[0,0,1]
	ds_read_b128 v[6:9], v231 offset:49152
	ds_read_b128 v[2:5], v235 offset:49152
	v_cmp_gt_i32_e32 vcc, s6, v222
	ds_write_b128 v12, v[14:17]
	ds_write_b128 v211, v[18:21]
	s_and_saveexec_b64 s[4:5], vcc
	s_cbranch_execz .LBB0_1082
	v_lshl_add_u64 v[12:13], v[10:11], 0, v[224:225]
	s_waitcnt lgkmcnt(0)
	global_store_dwordx4 v[12:13], v[6:9], off nt sc1
.LBB0_1082:
	s_or_b64 exec, exec, s[4:5]
	v_cmp_gt_i32_e32 vcc, s6, v226
	s_and_saveexec_b64 s[4:5], vcc
	s_cbranch_execz .LBB0_1084
	s_waitcnt lgkmcnt(0)
	v_lshl_add_u64 v[6:7], v[10:11], 0, v[228:229]
	global_store_dwordx4 v[6:7], v[2:5], off nt sc1

;     __device__ __forceinline__ void operator()(const f32x4 (&acc)[2][2][4][2], const Unit& u, int wr, int wc, int fr, int fq) const {
;     ...
;             const int rl = ai * 128 + mh * 32 + t0;
;             if (!nost) { if (rl < u.nv) __builtin_nontemporal_store(v0, (u32x4*)(yp + (size_t)rl * D)); if (rl + 4 < u.nv) __builtin_nontemporal_store(v1, (u32x4*)(yp + (size_t)(rl + 4) * D)); } }
.LBB0_1087:
	ds_read_b128 v[6:9], v248
	v_lshl_add_u64 v[12:13], v[10:11], 0, v[232:233]
	s_waitcnt lgkmcnt(0)
	global_store_dwordx4 v[12:13], v[6:9], off nt sc1
	s_or_b64 exec, exec, s[4:5]
	v_cmp_gt_i32_e32 vcc, s6, v234
	s_and_saveexec_b64 s[4:5], vcc
	s_cbranch_execz .LBB0_1086
.LBB0_1088:
	v_lshl_add_u64 v[6:7], v[10:11], 0, v[236:237]
	s_waitcnt lgkmcnt(0)
	global_store_dwordx4 v[6:7], v[2:5], off nt sc1
	s_or_b64 exec, exec, s[4:5]
	s_cmp_lg_u32 s3, s16
	s_mov_b64 s[4:5], -1
	s_cbranch_scc0 .LBB0_1062
